# grid barrier: non-leader WGs poll the top-level generation word directly instead of the per-XCD release word (one fewer hop)
# speedup vs baseline: 1.0146x; 1.0146x over previous
; __device__ __forceinline__ unsigned xb_ld(unsigned* p)              { return __hip_atomic_load(p, __ATOMIC_RELAXED, __HIP_MEMORY_SCOPE_AGENT); }
; __device__ __forceinline__ unsigned xb_add(unsigned* p, unsigned v) { return __hip_atomic_fetch_add(p, v, __ATOMIC_RELAXED, __HIP_MEMORY_SCOPE_AGENT); }
; #define XB_SPIN(cond, bar) do { unsigned _sp = 0; while (cond) { __builtin_amdgcn_s_sleep(1); \
;     if ((++_sp & 255u) == 0u) { if (xb_ld(&(bar)[XB_TMO])) break; if (_sp > XB_SPIN_CAP) { atomicAdd(&(bar)[XB_TMO], 1u); break; } } } } while (0)
; __device__ __forceinline__ void xcd_barrier(const XcdBarrier& b) {
;     ...
;     if (threadIdx.x == 0) {
;         unsigned* bar = b.bar;
;         __builtin_amdgcn_s_waitcnt(0);
;         unsigned nloc = b.st[0], nx = b.st[1];
;         if (nloc == 0u) { xcd_barrier_complete(bar, b.x, nloc, nx); b.st[0] = nloc; b.st[1] = nx; }
;         const unsigned old = xb_add(&bar[XB_XSUB(b.x)], 1u);
;         const unsigned gen = old / nloc;
;         if (old + 1u == (gen + 1u) * nloc) {
;             __builtin_amdgcn_fence(__ATOMIC_RELEASE, "agent");
;             asm volatile("s_waitcnt vmcnt(0)" ::: "memory");
;             const unsigned og = xb_add(&bar[XB_TOP], 1u);
;             const unsigned tg = og / nx;
;             if (og + 1u == (tg + 1u) * nx) xb_add(&bar[XB_TOPGEN], 1u);
;             else XB_SPIN(xb_ld(&bar[XB_TOPGEN]) == tg, bar);
;             __builtin_amdgcn_fence(__ATOMIC_ACQUIRE, "agent");
;             xb_add(&bar[XB_XGEN(b.x)], 1u);
;             asm volatile("s_waitcnt vmcnt(0)" ::: "memory");
;         } else {
;             XB_SPIN(xb_ld(&bar[XB_XGEN(b.x)]) == gen, bar);
;             __builtin_amdgcn_fence(__ATOMIC_ACQUIRE, "agent");
;             asm volatile("s_waitcnt vmcnt(0)" ::: "memory");
;         }
.LBB0_42:
	s_lshl_b32 s22, s33, 6
	s_add_i32 s4, s22, 0x500
	s_mov_b32 s5, 0
	s_lshl_b64 s[0:1], s[4:5], 2
	s_add_u32 s0, s38, s0
	s_addc_u32 s1, s39, s1
	v_mov_b32_e32 v1, 1
	v_mov_b64_e32 v[6:7], s[0:1]
	flat_atomic_add v1, v[6:7], v1 sc0
	v_cvt_f32_u32_e32 v3, v4
	v_sub_u32_e32 v5, 0, v4
	v_rcp_iflag_f32_e32 v3, v3
	s_nop 0
	v_mul_f32_e32 v3, 0x4f7ffffe, v3
	v_cvt_u32_f32_e32 v3, v3
	v_mul_lo_u32 v5, v5, v3
	v_mul_hi_u32 v5, v3, v5
	v_add_u32_e32 v3, v3, v5
	s_waitcnt vmcnt(0) lgkmcnt(0)
	v_mul_hi_u32 v3, v1, v3
	v_mul_lo_u32 v5, v3, v4
	v_add_u32_e32 v6, 1, v1
	v_sub_u32_e32 v1, v1, v5
	v_add_u32_e32 v7, 1, v3
	v_cmp_ge_u32_e32 vcc, v1, v4
	v_sub_u32_e32 v5, v1, v4
	s_nop 0
	v_cndmask_b32_e32 v3, v3, v7, vcc
	v_cndmask_b32_e32 v1, v1, v5, vcc
	v_add_u32_e32 v5, 1, v3
	v_cmp_ge_u32_e32 vcc, v1, v4
	s_nop 1
	v_cndmask_b32_e32 v1, v3, v5, vcc
	v_mad_u64_u32 v[4:5], s[0:1], v4, v1, v[4:5]
	v_cmp_ne_u32_e32 vcc, v6, v4
	s_and_saveexec_b64 s[0:1], vcc
	s_xor_b64 s[0:1], exec, s[0:1]
	s_cbranch_execz .LBB0_55
	s_add_i32 s4, s22, 0x900
	s_lshl_b64 s[4:5], s[4:5], 2
	s_add_u32 s6, s38, s4
	s_addc_u32 s7, s39, s5
	s_add_u32 s6, s38, 0x3500
	s_addc_u32 s7, s39, 0
	v_mov_b64_e32 v[2:3], s[6:7]
	flat_load_dword v2, v[2:3] sc1
	s_waitcnt vmcnt(0) lgkmcnt(0)
	v_cmp_eq_u32_e32 vcc, v2, v1
	s_and_saveexec_b64 s[4:5], vcc
	s_cbranch_execz .LBB0_54
	s_mov_b32 s23, 1
	s_mov_b64 s[8:9], 0
	s_branch .LBB0_46

; __device__ __forceinline__ unsigned xb_ld(unsigned* p)              { return __hip_atomic_load(p, __ATOMIC_RELAXED, __HIP_MEMORY_SCOPE_AGENT); }
; __device__ __forceinline__ unsigned xb_add(unsigned* p, unsigned v) { return __hip_atomic_fetch_add(p, v, __ATOMIC_RELAXED, __HIP_MEMORY_SCOPE_AGENT); }
; #define XB_SPIN(cond, bar) do { unsigned _sp = 0; while (cond) { __builtin_amdgcn_s_sleep(1); \
;     if ((++_sp & 255u) == 0u) { if (xb_ld(&(bar)[XB_TMO])) break; if (_sp > XB_SPIN_CAP) { atomicAdd(&(bar)[XB_TMO], 1u); break; } } } } while (0)
; __device__ __forceinline__ void xcd_barrier(const XcdBarrier& b) {
;     ...
;     if (threadIdx.x == 0) {
;         unsigned* bar = b.bar;
;         __builtin_amdgcn_s_waitcnt(0);
;         unsigned nloc = b.st[0], nx = b.st[1];
;         if (nloc == 0u) { xcd_barrier_complete(bar, b.x, nloc, nx); b.st[0] = nloc; b.st[1] = nx; }
;         const unsigned old = xb_add(&bar[XB_XSUB(b.x)], 1u);
;         const unsigned gen = old / nloc;
;         if (old + 1u == (gen + 1u) * nloc) {
;             __builtin_amdgcn_fence(__ATOMIC_RELEASE, "agent");
;             asm volatile("s_waitcnt vmcnt(0)" ::: "memory");
;             const unsigned og = xb_add(&bar[XB_TOP], 1u);
;             const unsigned tg = og / nx;
;             if (og + 1u == (tg + 1u) * nx) xb_add(&bar[XB_TOPGEN], 1u);
;             else XB_SPIN(xb_ld(&bar[XB_TOPGEN]) == tg, bar);
;             __builtin_amdgcn_fence(__ATOMIC_ACQUIRE, "agent");
;             xb_add(&bar[XB_XGEN(b.x)], 1u);
;             asm volatile("s_waitcnt vmcnt(0)" ::: "memory");
;         } else {
;             XB_SPIN(xb_ld(&bar[XB_XGEN(b.x)]) == gen, bar);
;             __builtin_amdgcn_fence(__ATOMIC_ACQUIRE, "agent");
;             asm volatile("s_waitcnt vmcnt(0)" ::: "memory");
;         }
.LBB0_177:
	s_lshl_b32 s22, s36, 6
	s_add_i32 s4, s22, 0x500
	s_mov_b32 s5, 0
	s_lshl_b64 s[0:1], s[4:5], 2
	s_add_u32 s0, s34, s0
	s_addc_u32 s1, s35, s1
	v_mov_b32_e32 v1, 1
	v_mov_b64_e32 v[6:7], s[0:1]
	flat_atomic_add v1, v[6:7], v1 sc0
	v_cvt_f32_u32_e32 v3, v4
	v_sub_u32_e32 v5, 0, v4
	v_rcp_iflag_f32_e32 v3, v3
	s_nop 0
	v_mul_f32_e32 v3, 0x4f7ffffe, v3
	v_cvt_u32_f32_e32 v3, v3
	v_mul_lo_u32 v5, v5, v3
	v_mul_hi_u32 v5, v3, v5
	v_add_u32_e32 v3, v3, v5
	s_waitcnt vmcnt(0) lgkmcnt(0)
	v_mul_hi_u32 v3, v1, v3
	v_mul_lo_u32 v5, v3, v4
	v_add_u32_e32 v6, 1, v1
	v_sub_u32_e32 v1, v1, v5
	v_add_u32_e32 v7, 1, v3
	v_cmp_ge_u32_e32 vcc, v1, v4
	v_sub_u32_e32 v5, v1, v4
	s_nop 0
	v_cndmask_b32_e32 v3, v3, v7, vcc
	v_cndmask_b32_e32 v1, v1, v5, vcc
	v_add_u32_e32 v5, 1, v3
	v_cmp_ge_u32_e32 vcc, v1, v4
	s_nop 1
	v_cndmask_b32_e32 v1, v3, v5, vcc
	v_mad_u64_u32 v[4:5], s[0:1], v4, v1, v[4:5]
	v_cmp_ne_u32_e32 vcc, v6, v4
	s_and_saveexec_b64 s[0:1], vcc
	s_xor_b64 s[0:1], exec, s[0:1]
	s_cbranch_execz .LBB0_190
	s_add_i32 s4, s22, 0x900
	s_lshl_b64 s[4:5], s[4:5], 2
	s_add_u32 s6, s34, s4
	s_addc_u32 s7, s35, s5
	s_add_u32 s6, s34, 0x3500
	s_addc_u32 s7, s35, 0
	v_mov_b64_e32 v[2:3], s[6:7]
	flat_load_dword v2, v[2:3] sc1
	s_waitcnt vmcnt(0) lgkmcnt(0)
	v_cmp_eq_u32_e32 vcc, v2, v1
	s_and_saveexec_b64 s[4:5], vcc
	s_cbranch_execz .LBB0_189
	s_mov_b32 s23, 1
	s_mov_b64 s[8:9], 0
	s_branch .LBB0_181

; __device__ __forceinline__ unsigned xb_ld(unsigned* p)              { return __hip_atomic_load(p, __ATOMIC_RELAXED, __HIP_MEMORY_SCOPE_AGENT); }
; __device__ __forceinline__ unsigned xb_add(unsigned* p, unsigned v) { return __hip_atomic_fetch_add(p, v, __ATOMIC_RELAXED, __HIP_MEMORY_SCOPE_AGENT); }
; #define XB_SPIN(cond, bar) do { unsigned _sp = 0; while (cond) { __builtin_amdgcn_s_sleep(1); \
;     if ((++_sp & 255u) == 0u) { if (xb_ld(&(bar)[XB_TMO])) break; if (_sp > XB_SPIN_CAP) { atomicAdd(&(bar)[XB_TMO], 1u); break; } } } } while (0)
; __device__ __forceinline__ void xcd_barrier(const XcdBarrier& b) {
;     ...
;     if (threadIdx.x == 0) {
;         unsigned* bar = b.bar;
;         __builtin_amdgcn_s_waitcnt(0);
;         unsigned nloc = b.st[0], nx = b.st[1];
;         if (nloc == 0u) { xcd_barrier_complete(bar, b.x, nloc, nx); b.st[0] = nloc; b.st[1] = nx; }
;         const unsigned old = xb_add(&bar[XB_XSUB(b.x)], 1u);
;         const unsigned gen = old / nloc;
;         if (old + 1u == (gen + 1u) * nloc) {
;             __builtin_amdgcn_fence(__ATOMIC_RELEASE, "agent");
;             asm volatile("s_waitcnt vmcnt(0)" ::: "memory");
;             const unsigned og = xb_add(&bar[XB_TOP], 1u);
;             const unsigned tg = og / nx;
;             if (og + 1u == (tg + 1u) * nx) xb_add(&bar[XB_TOPGEN], 1u);
;             else XB_SPIN(xb_ld(&bar[XB_TOPGEN]) == tg, bar);
;             __builtin_amdgcn_fence(__ATOMIC_ACQUIRE, "agent");
;             xb_add(&bar[XB_XGEN(b.x)], 1u);
;             asm volatile("s_waitcnt vmcnt(0)" ::: "memory");
;         } else {
;             XB_SPIN(xb_ld(&bar[XB_XGEN(b.x)]) == gen, bar);
;             __builtin_amdgcn_fence(__ATOMIC_ACQUIRE, "agent");
;             asm volatile("s_waitcnt vmcnt(0)" ::: "memory");
;         }
.LBB0_247:
	s_lshl_b32 s24, s36, 6
	s_add_i32 s4, s24, 0x500
	s_mov_b32 s5, 0
	s_lshl_b64 s[0:1], s[4:5], 2
	s_add_u32 s0, s34, s0
	s_addc_u32 s1, s35, s1
	v_mov_b32_e32 v1, 1
	v_mov_b64_e32 v[6:7], s[0:1]
	flat_atomic_add v1, v[6:7], v1 sc0
	v_cvt_f32_u32_e32 v3, v4
	v_sub_u32_e32 v5, 0, v4
	v_rcp_iflag_f32_e32 v3, v3
	s_nop 0
	v_mul_f32_e32 v3, 0x4f7ffffe, v3
	v_cvt_u32_f32_e32 v3, v3
	v_mul_lo_u32 v5, v5, v3
	v_mul_hi_u32 v5, v3, v5
	v_add_u32_e32 v3, v3, v5
	s_waitcnt vmcnt(0) lgkmcnt(0)
	v_mul_hi_u32 v3, v1, v3
	v_mul_lo_u32 v5, v3, v4
	v_add_u32_e32 v6, 1, v1
	v_sub_u32_e32 v1, v1, v5
	v_add_u32_e32 v7, 1, v3
	v_cmp_ge_u32_e32 vcc, v1, v4
	v_sub_u32_e32 v5, v1, v4
	s_nop 0
	v_cndmask_b32_e32 v3, v3, v7, vcc
	v_cndmask_b32_e32 v1, v1, v5, vcc
	v_add_u32_e32 v5, 1, v3
	v_cmp_ge_u32_e32 vcc, v1, v4
	s_nop 1
	v_cndmask_b32_e32 v1, v3, v5, vcc
	v_mad_u64_u32 v[4:5], s[0:1], v4, v1, v[4:5]
	v_cmp_ne_u32_e32 vcc, v6, v4
	s_and_saveexec_b64 s[0:1], vcc
	s_xor_b64 s[0:1], exec, s[0:1]
	s_cbranch_execz .LBB0_260
	s_add_i32 s4, s24, 0x900
	s_lshl_b64 s[4:5], s[4:5], 2
	s_add_u32 s6, s34, s4
	s_addc_u32 s7, s35, s5
	s_add_u32 s6, s34, 0x3500
	s_addc_u32 s7, s35, 0
	v_mov_b64_e32 v[2:3], s[6:7]
	flat_load_dword v2, v[2:3] sc1
	s_waitcnt vmcnt(0) lgkmcnt(0)
	v_cmp_eq_u32_e32 vcc, v2, v1
	s_and_saveexec_b64 s[4:5], vcc
	s_cbranch_execz .LBB0_259
	s_mov_b32 s22, 1
	s_mov_b64 s[8:9], 0
	s_branch .LBB0_251

; __device__ __forceinline__ unsigned xb_ld(unsigned* p)              { return __hip_atomic_load(p, __ATOMIC_RELAXED, __HIP_MEMORY_SCOPE_AGENT); }
; __device__ __forceinline__ unsigned xb_add(unsigned* p, unsigned v) { return __hip_atomic_fetch_add(p, v, __ATOMIC_RELAXED, __HIP_MEMORY_SCOPE_AGENT); }
; #define XB_SPIN(cond, bar) do { unsigned _sp = 0; while (cond) { __builtin_amdgcn_s_sleep(1); \
;     if ((++_sp & 255u) == 0u) { if (xb_ld(&(bar)[XB_TMO])) break; if (_sp > XB_SPIN_CAP) { atomicAdd(&(bar)[XB_TMO], 1u); break; } } } } while (0)
; __device__ __forceinline__ void xcd_barrier(const XcdBarrier& b) {
;     ...
;     if (threadIdx.x == 0) {
;         unsigned* bar = b.bar;
;         __builtin_amdgcn_s_waitcnt(0);
;         unsigned nloc = b.st[0], nx = b.st[1];
;         if (nloc == 0u) { xcd_barrier_complete(bar, b.x, nloc, nx); b.st[0] = nloc; b.st[1] = nx; }
;         const unsigned old = xb_add(&bar[XB_XSUB(b.x)], 1u);
;         const unsigned gen = old / nloc;
;         if (old + 1u == (gen + 1u) * nloc) {
;             __builtin_amdgcn_fence(__ATOMIC_RELEASE, "agent");
;             asm volatile("s_waitcnt vmcnt(0)" ::: "memory");
;             const unsigned og = xb_add(&bar[XB_TOP], 1u);
;             const unsigned tg = og / nx;
;             if (og + 1u == (tg + 1u) * nx) xb_add(&bar[XB_TOPGEN], 1u);
;             else XB_SPIN(xb_ld(&bar[XB_TOPGEN]) == tg, bar);
;             __builtin_amdgcn_fence(__ATOMIC_ACQUIRE, "agent");
;             xb_add(&bar[XB_XGEN(b.x)], 1u);
;             asm volatile("s_waitcnt vmcnt(0)" ::: "memory");
;         } else {
;             XB_SPIN(xb_ld(&bar[XB_XGEN(b.x)]) == gen, bar);
;             __builtin_amdgcn_fence(__ATOMIC_ACQUIRE, "agent");
;             asm volatile("s_waitcnt vmcnt(0)" ::: "memory");
;         }
.LBB0_346:
	s_lshl_b32 s22, s39, 6
	s_add_i32 s94, s22, 0x500
	s_lshl_b64 s[0:1], s[94:95], 2
	s_add_u32 s0, s36, s0
	s_addc_u32 s1, s37, s1
	v_mov_b64_e32 v[6:7], s[0:1]
	flat_atomic_add v3, v[6:7], v224 sc0
	v_cvt_f32_u32_e32 v1, v4
	v_sub_u32_e32 v5, 0, v4
	v_rcp_iflag_f32_e32 v1, v1
	s_nop 0
	v_mul_f32_e32 v1, 0x4f7ffffe, v1
	v_cvt_u32_f32_e32 v1, v1
	v_mul_lo_u32 v5, v5, v1
	v_mul_hi_u32 v5, v1, v5
	v_add_u32_e32 v1, v1, v5
	s_waitcnt vmcnt(0) lgkmcnt(0)
	v_mul_hi_u32 v1, v3, v1
	v_mul_lo_u32 v5, v1, v4
	v_sub_u32_e32 v5, v3, v5
	v_cmp_ge_u32_e32 vcc, v5, v4
	v_add_u32_e32 v6, 1, v1
	v_add_u32_e32 v3, 1, v3
	v_cndmask_b32_e32 v1, v1, v6, vcc
	v_sub_u32_e32 v6, v5, v4
	v_cndmask_b32_e32 v5, v5, v6, vcc
	v_cmp_ge_u32_e32 vcc, v5, v4
	v_add_u32_e32 v5, 1, v1
	s_nop 0
	v_cndmask_b32_e32 v1, v1, v5, vcc
	v_mad_u64_u32 v[4:5], s[0:1], v4, v1, v[4:5]
	v_cmp_ne_u32_e32 vcc, v3, v4
	s_and_saveexec_b64 s[0:1], vcc
	s_xor_b64 s[0:1], exec, s[0:1]
	s_cbranch_execz .LBB0_359
	s_add_i32 s94, s22, 0x900
	s_lshl_b64 s[4:5], s[94:95], 2
	s_add_u32 s6, s36, s4
	s_addc_u32 s7, s37, s5
	s_add_u32 s6, s36, 0x3500
	s_addc_u32 s7, s37, 0
	v_mov_b64_e32 v[2:3], s[6:7]
	flat_load_dword v2, v[2:3] sc1
	s_waitcnt vmcnt(0) lgkmcnt(0)
	v_cmp_eq_u32_e32 vcc, v2, v1
	s_and_saveexec_b64 s[4:5], vcc
	s_cbranch_execz .LBB0_358
	s_mov_b32 s23, 1
	s_mov_b64 s[8:9], 0
	s_branch .LBB0_350

; __device__ __forceinline__ unsigned xb_ld(unsigned* p)              { return __hip_atomic_load(p, __ATOMIC_RELAXED, __HIP_MEMORY_SCOPE_AGENT); }
; __device__ __forceinline__ unsigned xb_add(unsigned* p, unsigned v) { return __hip_atomic_fetch_add(p, v, __ATOMIC_RELAXED, __HIP_MEMORY_SCOPE_AGENT); }
; #define XB_SPIN(cond, bar) do { unsigned _sp = 0; while (cond) { __builtin_amdgcn_s_sleep(1); \
;     if ((++_sp & 255u) == 0u) { if (xb_ld(&(bar)[XB_TMO])) break; if (_sp > XB_SPIN_CAP) { atomicAdd(&(bar)[XB_TMO], 1u); break; } } } } while (0)
; __device__ __forceinline__ void xcd_barrier(const XcdBarrier& b) {
;     ...
;     if (threadIdx.x == 0) {
;         unsigned* bar = b.bar;
;         __builtin_amdgcn_s_waitcnt(0);
;         unsigned nloc = b.st[0], nx = b.st[1];
;         if (nloc == 0u) { xcd_barrier_complete(bar, b.x, nloc, nx); b.st[0] = nloc; b.st[1] = nx; }
;         const unsigned old = xb_add(&bar[XB_XSUB(b.x)], 1u);
;         const unsigned gen = old / nloc;
;         if (old + 1u == (gen + 1u) * nloc) {
;             __builtin_amdgcn_fence(__ATOMIC_RELEASE, "agent");
;             asm volatile("s_waitcnt vmcnt(0)" ::: "memory");
;             const unsigned og = xb_add(&bar[XB_TOP], 1u);
;             const unsigned tg = og / nx;
;             if (og + 1u == (tg + 1u) * nx) xb_add(&bar[XB_TOPGEN], 1u);
;             else XB_SPIN(xb_ld(&bar[XB_TOPGEN]) == tg, bar);
;             __builtin_amdgcn_fence(__ATOMIC_ACQUIRE, "agent");
;             xb_add(&bar[XB_XGEN(b.x)], 1u);
;             asm volatile("s_waitcnt vmcnt(0)" ::: "memory");
;         } else {
;             XB_SPIN(xb_ld(&bar[XB_XGEN(b.x)]) == gen, bar);
;             __builtin_amdgcn_fence(__ATOMIC_ACQUIRE, "agent");
;             asm volatile("s_waitcnt vmcnt(0)" ::: "memory");
;         }
.LBB0_416:
	s_lshl_b32 s24, s39, 6
	s_add_i32 s94, s24, 0x500
	s_lshl_b64 s[0:1], s[94:95], 2
	s_add_u32 s0, s36, s0
	s_addc_u32 s1, s37, s1
	v_mov_b64_e32 v[6:7], s[0:1]
	flat_atomic_add v3, v[6:7], v224 sc0
	v_cvt_f32_u32_e32 v1, v4
	v_sub_u32_e32 v5, 0, v4
	v_rcp_iflag_f32_e32 v1, v1
	s_nop 0
	v_mul_f32_e32 v1, 0x4f7ffffe, v1
	v_cvt_u32_f32_e32 v1, v1
	v_mul_lo_u32 v5, v5, v1
	v_mul_hi_u32 v5, v1, v5
	v_add_u32_e32 v1, v1, v5
	s_waitcnt vmcnt(0) lgkmcnt(0)
	v_mul_hi_u32 v1, v3, v1
	v_mul_lo_u32 v5, v1, v4
	v_sub_u32_e32 v5, v3, v5
	v_cmp_ge_u32_e32 vcc, v5, v4
	v_add_u32_e32 v6, 1, v1
	v_add_u32_e32 v3, 1, v3
	v_cndmask_b32_e32 v1, v1, v6, vcc
	v_sub_u32_e32 v6, v5, v4
	v_cndmask_b32_e32 v5, v5, v6, vcc
	v_cmp_ge_u32_e32 vcc, v5, v4
	v_add_u32_e32 v5, 1, v1
	s_nop 0
	v_cndmask_b32_e32 v1, v1, v5, vcc
	v_mad_u64_u32 v[4:5], s[0:1], v4, v1, v[4:5]
	v_cmp_ne_u32_e32 vcc, v3, v4
	s_and_saveexec_b64 s[0:1], vcc
	s_xor_b64 s[0:1], exec, s[0:1]
	s_cbranch_execz .LBB0_429
	s_add_i32 s94, s24, 0x900
	s_lshl_b64 s[4:5], s[94:95], 2
	s_add_u32 s6, s36, s4
	s_addc_u32 s7, s37, s5
	s_add_u32 s6, s36, 0x3500
	s_addc_u32 s7, s37, 0
	v_mov_b64_e32 v[2:3], s[6:7]
	flat_load_dword v2, v[2:3] sc1
	s_waitcnt vmcnt(0) lgkmcnt(0)
	v_cmp_eq_u32_e32 vcc, v2, v1
	s_and_saveexec_b64 s[4:5], vcc
	s_cbranch_execz .LBB0_428
	s_mov_b32 s22, 1
	s_mov_b64 s[8:9], 0
	s_branch .LBB0_420

; __device__ __forceinline__ unsigned xb_ld(unsigned* p)              { return __hip_atomic_load(p, __ATOMIC_RELAXED, __HIP_MEMORY_SCOPE_AGENT); }
; __device__ __forceinline__ unsigned xb_add(unsigned* p, unsigned v) { return __hip_atomic_fetch_add(p, v, __ATOMIC_RELAXED, __HIP_MEMORY_SCOPE_AGENT); }
; #define XB_SPIN(cond, bar) do { unsigned _sp = 0; while (cond) { __builtin_amdgcn_s_sleep(1); \
;     if ((++_sp & 255u) == 0u) { if (xb_ld(&(bar)[XB_TMO])) break; if (_sp > XB_SPIN_CAP) { atomicAdd(&(bar)[XB_TMO], 1u); break; } } } } while (0)
; __device__ __forceinline__ void xcd_barrier(const XcdBarrier& b) {
;     ...
;     if (threadIdx.x == 0) {
;         unsigned* bar = b.bar;
;         __builtin_amdgcn_s_waitcnt(0);
;         unsigned nloc = b.st[0], nx = b.st[1];
;         if (nloc == 0u) { xcd_barrier_complete(bar, b.x, nloc, nx); b.st[0] = nloc; b.st[1] = nx; }
;         const unsigned old = xb_add(&bar[XB_XSUB(b.x)], 1u);
;         const unsigned gen = old / nloc;
;         if (old + 1u == (gen + 1u) * nloc) {
;             __builtin_amdgcn_fence(__ATOMIC_RELEASE, "agent");
;             asm volatile("s_waitcnt vmcnt(0)" ::: "memory");
;             const unsigned og = xb_add(&bar[XB_TOP], 1u);
;             const unsigned tg = og / nx;
;             if (og + 1u == (tg + 1u) * nx) xb_add(&bar[XB_TOPGEN], 1u);
;             else XB_SPIN(xb_ld(&bar[XB_TOPGEN]) == tg, bar);
;             __builtin_amdgcn_fence(__ATOMIC_ACQUIRE, "agent");
;             xb_add(&bar[XB_XGEN(b.x)], 1u);
;             asm volatile("s_waitcnt vmcnt(0)" ::: "memory");
;         } else {
;             XB_SPIN(xb_ld(&bar[XB_XGEN(b.x)]) == gen, bar);
;             __builtin_amdgcn_fence(__ATOMIC_ACQUIRE, "agent");
;             asm volatile("s_waitcnt vmcnt(0)" ::: "memory");
;         }
.LBB0_2013:
	s_lshl_b32 s22, s37, 6
	s_add_i32 s94, s22, 0x500
	s_lshl_b64 s[0:1], s[94:95], 2
	s_add_u32 s0, s34, s0
	s_addc_u32 s1, s35, s1
	v_mov_b64_e32 v[6:7], s[0:1]
	flat_atomic_add v3, v[6:7], v224 sc0
	v_cvt_f32_u32_e32 v1, v4
	v_sub_u32_e32 v5, 0, v4
	v_rcp_iflag_f32_e32 v1, v1
	s_nop 0
	v_mul_f32_e32 v1, 0x4f7ffffe, v1
	v_cvt_u32_f32_e32 v1, v1
	v_mul_lo_u32 v5, v5, v1
	v_mul_hi_u32 v5, v1, v5
	v_add_u32_e32 v1, v1, v5
	s_waitcnt vmcnt(0) lgkmcnt(0)
	v_mul_hi_u32 v1, v3, v1
	v_mul_lo_u32 v5, v1, v4
	v_sub_u32_e32 v5, v3, v5
	v_cmp_ge_u32_e32 vcc, v5, v4
	v_add_u32_e32 v6, 1, v1
	v_add_u32_e32 v3, 1, v3
	v_cndmask_b32_e32 v1, v1, v6, vcc
	v_sub_u32_e32 v6, v5, v4
	v_cndmask_b32_e32 v5, v5, v6, vcc
	v_cmp_ge_u32_e32 vcc, v5, v4
	v_add_u32_e32 v5, 1, v1
	s_nop 0
	v_cndmask_b32_e32 v1, v1, v5, vcc
	v_mad_u64_u32 v[4:5], s[0:1], v4, v1, v[4:5]
	v_cmp_ne_u32_e32 vcc, v3, v4
	s_and_saveexec_b64 s[0:1], vcc
	v_readlane_b32 s30, v255, 3
	s_xor_b64 s[0:1], exec, s[0:1]
	v_readlane_b32 s31, v255, 4
	s_cbranch_execz .LBB0_2026
	s_add_i32 s94, s22, 0x900
	s_lshl_b64 s[4:5], s[94:95], 2
	s_add_u32 s6, s34, s4
	s_addc_u32 s7, s35, s5
	s_add_u32 s6, s34, 0x3500
	s_addc_u32 s7, s35, 0
	v_mov_b64_e32 v[2:3], s[6:7]
	flat_load_dword v2, v[2:3] sc1
	s_waitcnt vmcnt(0) lgkmcnt(0)
	v_cmp_eq_u32_e32 vcc, v2, v1
	s_and_saveexec_b64 s[4:5], vcc
	s_cbranch_execz .LBB0_2025
	s_mov_b32 s23, 1
	s_mov_b64 s[8:9], 0
	s_branch .LBB0_2017

; __device__ __forceinline__ unsigned xb_ld(unsigned* p)              { return __hip_atomic_load(p, __ATOMIC_RELAXED, __HIP_MEMORY_SCOPE_AGENT); }
; __device__ __forceinline__ unsigned xb_add(unsigned* p, unsigned v) { return __hip_atomic_fetch_add(p, v, __ATOMIC_RELAXED, __HIP_MEMORY_SCOPE_AGENT); }
; #define XB_SPIN(cond, bar) do { unsigned _sp = 0; while (cond) { __builtin_amdgcn_s_sleep(1); \
;     if ((++_sp & 255u) == 0u) { if (xb_ld(&(bar)[XB_TMO])) break; if (_sp > XB_SPIN_CAP) { atomicAdd(&(bar)[XB_TMO], 1u); break; } } } } while (0)
; __device__ __forceinline__ void xcd_barrier(const XcdBarrier& b) {
;     ...
;     if (threadIdx.x == 0) {
;         unsigned* bar = b.bar;
;         __builtin_amdgcn_s_waitcnt(0);
;         unsigned nloc = b.st[0], nx = b.st[1];
;         if (nloc == 0u) { xcd_barrier_complete(bar, b.x, nloc, nx); b.st[0] = nloc; b.st[1] = nx; }
;         const unsigned old = xb_add(&bar[XB_XSUB(b.x)], 1u);
;         const unsigned gen = old / nloc;
;         if (old + 1u == (gen + 1u) * nloc) {
;             __builtin_amdgcn_fence(__ATOMIC_RELEASE, "agent");
;             asm volatile("s_waitcnt vmcnt(0)" ::: "memory");
;             const unsigned og = xb_add(&bar[XB_TOP], 1u);
;             const unsigned tg = og / nx;
;             if (og + 1u == (tg + 1u) * nx) xb_add(&bar[XB_TOPGEN], 1u);
;             else XB_SPIN(xb_ld(&bar[XB_TOPGEN]) == tg, bar);
;             __builtin_amdgcn_fence(__ATOMIC_ACQUIRE, "agent");
;             xb_add(&bar[XB_XGEN(b.x)], 1u);
;             asm volatile("s_waitcnt vmcnt(0)" ::: "memory");
;         } else {
;             XB_SPIN(xb_ld(&bar[XB_XGEN(b.x)]) == gen, bar);
;             __builtin_amdgcn_fence(__ATOMIC_ACQUIRE, "agent");
;             asm volatile("s_waitcnt vmcnt(0)" ::: "memory");
;         }
.LBB0_2083:
	s_lshl_b32 s24, s37, 6
	s_add_i32 s94, s24, 0x500
	s_lshl_b64 s[0:1], s[94:95], 2
	s_add_u32 s0, s34, s0
	s_addc_u32 s1, s35, s1
	v_mov_b64_e32 v[6:7], s[0:1]
	flat_atomic_add v3, v[6:7], v224 sc0
	v_cvt_f32_u32_e32 v1, v4
	v_sub_u32_e32 v5, 0, v4
	v_rcp_iflag_f32_e32 v1, v1
	s_nop 0
	v_mul_f32_e32 v1, 0x4f7ffffe, v1
	v_cvt_u32_f32_e32 v1, v1
	v_mul_lo_u32 v5, v5, v1
	v_mul_hi_u32 v5, v1, v5
	v_add_u32_e32 v1, v1, v5
	s_waitcnt vmcnt(0) lgkmcnt(0)
	v_mul_hi_u32 v1, v3, v1
	v_mul_lo_u32 v5, v1, v4
	v_sub_u32_e32 v5, v3, v5
	v_cmp_ge_u32_e32 vcc, v5, v4
	v_add_u32_e32 v6, 1, v1
	v_add_u32_e32 v3, 1, v3
	v_cndmask_b32_e32 v1, v1, v6, vcc
	v_sub_u32_e32 v6, v5, v4
	v_cndmask_b32_e32 v5, v5, v6, vcc
	v_cmp_ge_u32_e32 vcc, v5, v4
	v_add_u32_e32 v5, 1, v1
	s_nop 0
	v_cndmask_b32_e32 v1, v1, v5, vcc
	v_mad_u64_u32 v[4:5], s[0:1], v4, v1, v[4:5]
	v_cmp_ne_u32_e32 vcc, v3, v4
	s_and_saveexec_b64 s[0:1], vcc
	v_readlane_b32 s30, v255, 3
	s_xor_b64 s[0:1], exec, s[0:1]
	v_readlane_b32 s31, v255, 4
	s_cbranch_execz .LBB0_2096
	s_add_i32 s94, s24, 0x900
	s_lshl_b64 s[4:5], s[94:95], 2
	s_add_u32 s6, s34, s4
	s_addc_u32 s7, s35, s5
	s_add_u32 s6, s34, 0x3500
	s_addc_u32 s7, s35, 0
	v_mov_b64_e32 v[2:3], s[6:7]
	flat_load_dword v2, v[2:3] sc1
	s_waitcnt vmcnt(0) lgkmcnt(0)
	v_cmp_eq_u32_e32 vcc, v2, v1
	s_and_saveexec_b64 s[4:5], vcc
	s_cbranch_execz .LBB0_2095
	s_mov_b32 s22, 1
	s_mov_b64 s[8:9], 0
	s_branch .LBB0_2087
